# T10 variant: 6144 items moved, waves 1..3, one half-item unit per wave per seam
# baseline (speedup 1.0000x reference)
; __device__ __forceinline__ unsigned pk4_fp8(float a, float b, float c, float d) { int w = 0; w = __builtin_amdgcn_cvt_pk_fp8_f32(clamp448(a), clamp448(b), w, false); w = __builtin_amdgcn_cvt_pk_fp8_f32(clamp448(c), clamp448(d), w, true); return (unsigned)w; }
; __device__ __forceinline__ void transpose_item_f8(const float* W, int N, unsigned char* WT, int ldt, int kind, int off, int item, int lane, float scale) {
;     const int nblk = N >> 6, kb = item / nblk, nb = item - kb * nblk, k0 = 128 * kb + 16 * (lane & 7), n = 64 * nb + 4 * (lane >> 3);
;     const f32x4* src = (const f32x4*)(W + (size_t)k0 * N + n);
;     f32x4 v[2][16];
; #pragma unroll
;     for (int hh = 0; hh < 2; ++hh)
; #pragma unroll
;         for (int j = 0; j < 16; ++j) v[hh][j] = __builtin_nontemporal_load(src + (size_t)j * (N >> 2) + 8 * hh);
; #pragma unroll
;     for (int hh = 0; hh < 2; ++hh)
; #pragma unroll
;         for (int i = 0; i < 4; ++i) { v4u o; o.x = pg8::pk4_fp8(v[hh][0][i] * scale, v[hh][1][i] * scale, v[hh][2][i] * scale, v[hh][3][i] * scale); o.y = pg8::pk4_fp8(v[hh][4][i] * scale, v[hh][5][i] * scale, v[hh][6][i] * scale, v[hh][7][i] * scale);
; __device__ __forceinline__ void moe_convert(Frame& F, int lo, int hi, int rank, int nrank) {
;     ...
;     for (int it = lo + rank; it < hi; it += nrank) {
;         int r = it; const float* W; unsigned char* WT; int N, ldt, kind, off; float f8s;
;         if (r < 14336) { const int e = r / 1792; r -= e * 1792; W = F.in[IN_WMG] + (size_t)e * 2048 * DFFE; N = DFFE; WT = F.ws + WS_WGU1 + (size_t)e * 14336 * 2048; ldt = 2048; kind = 1; off = 0; f8s = 32.f; }
;         else if ((r -= 14336) < 14336) { const int e = r / 1792; r -= e * 1792; W = F.in[IN_WMU] + (size_t)e * 2048 * DFFE; N = DFFE; WT = F.ws + WS_WGU1 + (size_t)e * 14336 * 2048; ldt = 2048; kind = 1; off = 128; f8s = 256.f; }
;         else { r -= 14336; const int e = r / 1792; r -= e * 1792; W = F.in[IN_WMD] + (size_t)e * DFFE * 2048; N = 2048; WT = F.ws + WS_WDN1 + (size_t)e * 2048 * DFFE; ldt = DFFE; kind = 0; off = 0; f8s = 64.f; }
;         transpose_item_f8(W, N, WT, ldt, kind, off, r, F.lane, f8s);
.LBB0_235:
	s_cmp_gt_i32 s24, 0x6fff
	s_cbranch_scc1 .LBB0_246
	s_add_u32 s14, s86, 0x23800000
	s_addc_u32 s15, s87, 0
	v_lshlrev_b32_e32 v1, 4, v0
	s_waitcnt vmcnt(2)
	v_lshrrev_b32_e32 v2, 1, v0
	s_add_u32 s16, s86, 0x7800000
	v_and_b32_e32 v1, 0x70, v1
	v_and_b32_e32 v134, 28, v2
	s_addc_u32 s17, s87, 0
	s_add_i32 s18, s24, 0xffff9000
	s_mov_b32 s3, 0
	s_mov_b32 s19, 0xc3e00000
	v_mov_b32_e32 v135, 0x43e00000
	v_mov_b32_e32 v136, 0x5c
	s_movk_i32 s20, 0x5d
	s_movk_i32 s21, 0x5e
	s_movk_i32 s22, 0x5f
	s_movk_i32 s23, 0x7c
	s_movk_i32 s26, 0x7d
	s_movk_i32 s27, 0x7e
	s_movk_i32 s28, 0x7f
	s_mov_b32 s29, s24
	s_branch .LBB0_238
.LBB0_237:
	s_lshr_b32 s12, s2, 6
	v_cvt_f32_u32_e32 v2, s12
	s_sub_i32 s35, 0, s12
	s_abs_i32 s34, s33
	s_ashr_i32 s13, s33, 31
	v_rcp_iflag_f32_e32 v2, v2
	v_mov_b32_e32 v138, 0
	v_mov_b32_e32 v139, 0
	v_mov_b32_e32 v140, 0
	v_mul_f32_e32 v2, 0x4f7ffffe, v2
	v_cvt_u32_f32_e32 v2, v2
	v_mov_b32_e32 v141, 0
	v_readfirstlane_b32 s36, v2
	s_mul_i32 s35, s35, s36
	s_mul_hi_u32 s35, s36, s35
	s_add_i32 s36, s36, s35
	s_mul_hi_u32 s35, s34, s36
	s_mul_i32 s36, s35, s12
	s_sub_i32 s34, s34, s36
	s_add_i32 s37, s35, 1
	s_sub_i32 s36, s34, s12
	s_cmp_ge_u32 s34, s12
	s_cselect_b32 s35, s37, s35
	s_cselect_b32 s34, s36, s34
	s_add_i32 s36, s35, 1
	s_cmp_ge_u32 s34, s12
	s_cselect_b32 s34, s36, s35
	s_xor_b32 s34, s34, s13
	s_sub_i32 s13, s34, s13
	v_lshl_or_b32 v132, s13, 7, v1
	s_mul_i32 s12, s13, s12
	v_mad_u64_u32 v[2:3], s[34:35], v132, s2, 0
	s_sub_i32 s12, s33, s12
	v_ashrrev_i32_e32 v133, 31, v132
	v_mov_b32_e32 v4, v3
	s_lshl_b32 s13, s12, 6
	v_mad_u64_u32 v[4:5], s[34:35], v133, s2, v[4:5]
	v_or_b32_e32 v130, s13, v134
	v_mov_b32_e32 v3, v4
	v_lshl_add_u64 v[2:3], v[2:3], 2, s[10:11]
	v_ashrrev_i32_e32 v131, 31, v130
	v_lshl_add_u64 v[2:3], v[130:131], 2, v[2:3]
	s_lshr_b32 s10, s2, 2
	s_mov_b32 s11, s3
	v_lshl_add_u64 v[4:5], s[10:11], 4, v[2:3]
	s_lshr_b32 s34, s2, 1
	s_mov_b32 s35, s3
	global_load_dwordx4 v[66:69], v[2:3], off nt
	global_load_dwordx4 v[70:73], v[4:5], off nt
	s_waitcnt vmcnt(2)
	v_lshl_add_u64 v[6:7], s[34:35], 4, v[2:3]
	s_mul_i32 s34, s10, 3
	s_mul_i32 s36, s10, 6
	s_mov_b32 s37, s3
	v_lshl_add_u64 v[8:9], s[34:35], 4, v[2:3]
	s_ashr_i32 s35, s2, 31
	s_mov_b32 s34, s2
	v_lshl_add_u64 v[12:13], s[36:37], 4, v[2:3]
	s_mul_i32 s36, s10, 7
	v_lshl_add_u64 v[10:11], s[2:3], 4, v[2:3]
	v_lshl_add_u64 v[14:15], s[36:37], 4, v[2:3]
	v_lshl_add_u64 v[16:17], s[34:35], 4, v[4:5]
	global_load_dwordx4 v[74:77], v[10:11], off nt
	global_load_dwordx4 v[90:93], v[12:13], off nt
	global_load_dwordx4 v[86:89], v[14:15], off nt
	global_load_dwordx4 v[102:105], v[16:17], off nt
	s_lshl_b32 s2, s2, 1
	global_load_dwordx4 v[82:85], v[6:7], off nt
	global_load_dwordx4 v[78:81], v[8:9], off nt
	v_lshl_add_u64 v[18:19], s[2:3], 4, v[2:3]
	s_mul_i32 s2, s10, 9
	v_lshl_add_u64 v[20:21], s[2:3], 4, v[2:3]
	global_load_dwordx4 v[94:97], v[18:19], off nt
	global_load_dwordx4 v[98:101], v[20:21], off nt
	s_mul_i32 s2, s10, 10
	v_lshl_add_u64 v[54:55], s[2:3], 4, v[2:3]
	s_mul_i32 s2, s10, 11
	v_lshl_add_u64 v[56:57], s[2:3], 4, v[2:3]
	s_mul_i32 s2, s10, 12
	global_load_dwordx4 v[114:117], v[54:55], off nt
	global_load_dwordx4 v[106:109], v[56:57], off nt
	v_lshl_add_u64 v[58:59], s[2:3], 4, v[2:3]
	s_mul_i32 s2, s10, 13
	v_lshl_add_u64 v[60:61], s[2:3], 4, v[2:3]
	global_load_dwordx4 v[110:113], v[58:59], off nt
	global_load_dwordx4 v[118:121], v[60:61], off nt
	s_mul_i32 s2, s10, 14
	v_lshl_add_u64 v[62:63], s[2:3], 4, v[2:3]
	s_mul_i32 s2, s10, 15
	v_lshl_add_u64 v[142:143], s[2:3], 4, v[2:3]
	global_load_dwordx4 v[122:125], v[62:63], off nt
	global_load_dwordx4 v[126:129], v[142:143], off nt
	global_load_dwordx4 v[42:45], v[2:3], off offset:128 nt
	global_load_dwordx4 v[46:49], v[4:5], off offset:128 nt
	global_load_dwordx4 v[50:53], v[6:7], off offset:128 nt
	global_load_dwordx4 v[38:41], v[8:9], off offset:128 nt
	global_load_dwordx4 v[30:33], v[10:11], off offset:128 nt
	global_load_dwordx4 v[26:29], v[12:13], off offset:128 nt
	global_load_dwordx4 v[22:25], v[14:15], off offset:128 nt
	global_load_dwordx4 v[34:37], v[16:17], off offset:128 nt
	s_nop 0
	global_load_dwordx4 v[10:13], v[18:19], off offset:128 nt
	global_load_dwordx4 v[14:17], v[20:21], off offset:128 nt
	s_nop 0
	global_load_dwordx4 v[18:21], v[54:55], off offset:128 nt
	global_load_dwordx4 v[6:9], v[56:57], off offset:128 nt
	global_load_dwordx4 v[2:5], v[58:59], off offset:128 nt
	s_lshl_b32 s2, s12, 7
	s_and_b32 s2, s2, 0xffffff00
	s_or_b32 s2, s2, s30
	v_lshl_add_u64 v[132:133], s[8:9], 0, v[132:133]
	s_add_i32 s29, s29, s25
	s_add_i32 s18, s18, s25
	s_cmp_lt_i32 s29, 0x7000
	s_waitcnt vmcnt(28)
	v_mul_f32_e32 v54, s31, v66
	s_waitcnt vmcnt(27)
	v_mul_f32_e32 v55, s31, v70
	v_med3_f32 v54, v54, s19, v135
	v_med3_f32 v55, v55, s19, v135
	v_cvt_pk_fp8_f32 v138, v54, v55
	s_waitcnt vmcnt(26)
	v_mul_f32_e32 v58, s31, v74
	v_med3_f32 v58, v58, s19, v135
	s_waitcnt vmcnt(25)
	v_mul_f32_e32 v59, s31, v90
	s_waitcnt vmcnt(23)
	v_mul_f32_e32 v65, s31, v102
	v_med3_f32 v54, v65, s19, v135
	s_waitcnt vmcnt(22)
	v_mul_f32_e32 v56, s31, v82
	s_waitcnt vmcnt(21)
	v_mul_f32_e32 v57, s31, v78
	v_cvt_pk_fp8_f32 v139, v58, v54
	v_med3_f32 v54, v56, s19, v135
	v_med3_f32 v55, v57, s19, v135
	v_cvt_pk_fp8_f32 v138, v54, v55 op_sel:[0,0,1]
	s_waitcnt vmcnt(20)
	v_mul_f32_e32 v54, s31, v94
	s_waitcnt vmcnt(19)
	v_mul_f32_e32 v55, s31, v98
	v_med3_f32 v54, v54, s19, v135
	v_med3_f32 v55, v55, s19, v135
	v_mul_f32_e32 v64, s31, v86
	v_cvt_pk_fp8_f32 v140, v54, v55
	v_med3_f32 v56, v59, s19, v135
	v_med3_f32 v57, v64, s19, v135
	v_cvt_pk_fp8_f32 v139, v56, v57 op_sel:[0,0,1]
	s_waitcnt vmcnt(18)
; __device__ __forceinline__ unsigned pk4_fp8(float a, float b, float c, float d) { int w = 0; w = __builtin_amdgcn_cvt_pk_fp8_f32(clamp448(a), clamp448(b), w, false); w = __builtin_amdgcn_cvt_pk_fp8_f32(clamp448(c), clamp448(d), w, true); return (unsigned)w; }
; __device__ __forceinline__ void transpose_item_f8(const float* W, int N, unsigned char* WT, int ldt, int kind, int off, int item, int lane, float scale) {
;     ...
;     for (int hh = 0; hh < 2; ++hh)
; #pragma unroll
;         for (int i = 0; i < 4; ++i) { v4u o; o.x = pg8::pk4_fp8(v[hh][0][i] * scale, v[hh][1][i] * scale, v[hh][2][i] * scale, v[hh][3][i] * scale); o.y = pg8::pk4_fp8(v[hh][4][i] * scale, v[hh][5][i] * scale, v[hh][6][i] * scale, v[hh][7][i] * scale);
;             o.z = pg8::pk4_fp8(v[hh][8][i] * scale, v[hh][9][i] * scale, v[hh][10][i] * scale, v[hh][11][i] * scale); o.w = pg8::pk4_fp8(v[hh][12][i] * scale, v[hh][13][i] * scale, v[hh][14][i] * scale, v[hh][15][i] * scale);
;             __builtin_nontemporal_store(o, (v4u*)(WT + (size_t)rowmap(kind, off, n + 32 * hh + i) * ldt + k0)); }
	v_mul_f32_e32 v56, s31, v114
	s_waitcnt vmcnt(17)
	v_mul_f32_e32 v54, s31, v106
	v_med3_f32 v55, v56, s19, v135
	v_med3_f32 v54, v54, s19, v135
	v_cvt_pk_fp8_f32 v140, v55, v54 op_sel:[0,0,1]
	s_waitcnt vmcnt(16)
	v_mul_f32_e32 v54, s31, v110
	s_waitcnt vmcnt(15)
	v_mul_f32_e32 v59, s31, v118
	v_med3_f32 v58, v54, s19, v135
	v_med3_f32 v59, v59, s19, v135
	v_cvt_pk_fp8_f32 v141, v58, v59
	s_waitcnt vmcnt(14)
	v_mul_f32_e32 v58, s31, v122
	s_waitcnt vmcnt(13)
	v_mul_f32_e32 v70, s31, v126
	v_med3_f32 v66, v58, s19, v135
	v_med3_f32 v70, v70, s19, v135
	v_cvt_pk_fp8_f32 v141, v66, v70 op_sel:[0,0,1]
	v_bitop3_b32 v66, s13, v136, v134 bitop3:0xc8
	v_or_b32_e32 v66, s2, v66
	v_add_u32_e32 v70, s30, v130
	v_cndmask_b32_e64 v66, v66, v70, s[4:5]
	v_ashrrev_i32_e32 v70, 31, v66
	global_load_dwordx4 v[54:57], v[60:61], off offset:128 nt
	v_mul_lo_u32 v70, s6, v70
	global_load_dwordx4 v[62:65], v[62:63], off offset:128 nt
	v_mul_lo_u32 v74, s7, v66
	global_load_dwordx4 v[58:61], v[142:143], off offset:128 nt
	v_mad_u64_u32 v[142:143], s[8:9], s6, v66, v[132:133]
	v_add3_u32 v143, v74, v143, v70
	v_mul_f32_e32 v66, s31, v67
	v_mul_f32_e32 v67, s31, v71
	global_store_dwordx4 v[142:143], v[138:141], off nt
	v_med3_f32 v66, v66, s19, v135
	v_med3_f32 v67, v67, s19, v135
	v_mov_b32_e32 v138, 0
	v_cvt_pk_fp8_f32 v138, v66, v67
	v_mul_f32_e32 v66, s31, v83
	v_mul_f32_e32 v67, s31, v79
	v_med3_f32 v66, v66, s19, v135
	v_med3_f32 v67, v67, s19, v135
	v_cvt_pk_fp8_f32 v138, v66, v67 op_sel:[0,0,1]
	v_mul_f32_e32 v66, s31, v75
	v_mul_f32_e32 v67, s31, v103
	v_med3_f32 v66, v66, s19, v135
	v_med3_f32 v67, v67, s19, v135
	v_mov_b32_e32 v139, 0
	v_cvt_pk_fp8_f32 v139, v66, v67
	v_mul_f32_e32 v66, s31, v91
	v_mul_f32_e32 v67, s31, v87
	v_med3_f32 v66, v66, s19, v135
	v_med3_f32 v67, v67, s19, v135
	v_cvt_pk_fp8_f32 v139, v66, v67 op_sel:[0,0,1]
	v_mul_f32_e32 v66, s31, v95
	v_mul_f32_e32 v67, s31, v99
	v_med3_f32 v66, v66, s19, v135
	v_med3_f32 v67, v67, s19, v135
	v_mov_b32_e32 v140, 0
	v_cvt_pk_fp8_f32 v140, v66, v67
	v_mul_f32_e32 v66, s31, v115
	v_mul_f32_e32 v67, s31, v107
	v_med3_f32 v66, v66, s19, v135
	v_med3_f32 v67, v67, s19, v135
	v_cvt_pk_fp8_f32 v140, v66, v67 op_sel:[0,0,1]
	v_mul_f32_e32 v66, s31, v111
	v_mul_f32_e32 v67, s31, v119
	v_med3_f32 v66, v66, s19, v135
	v_med3_f32 v67, v67, s19, v135
	v_mov_b32_e32 v141, 0
	v_cvt_pk_fp8_f32 v141, v66, v67
	v_mul_f32_e32 v66, s31, v123
	v_mul_f32_e32 v67, s31, v127
	v_med3_f32 v66, v66, s19, v135
	v_med3_f32 v67, v67, s19, v135
	v_cvt_pk_fp8_f32 v141, v66, v67 op_sel:[0,0,1]
	v_or_b32_e32 v66, 1, v130
	v_bitop3_b32 v67, v130, s20, 1 bitop3:0xc8
	v_add_u32_e32 v66, s30, v66
	v_or_b32_e32 v67, s2, v67
	v_cndmask_b32_e64 v66, v67, v66, s[4:5]
	v_ashrrev_i32_e32 v67, 31, v66
	v_mul_lo_u32 v70, s6, v67
	v_mul_lo_u32 v71, s7, v66
	v_mad_u64_u32 v[66:67], s[8:9], s6, v66, v[132:133]
	v_add3_u32 v67, v71, v67, v70
	global_store_dwordx4 v[66:67], v[138:141], off nt
	v_mul_f32_e32 v66, s31, v68
	v_mul_f32_e32 v67, s31, v72
	v_med3_f32 v66, v66, s19, v135
	v_med3_f32 v67, v67, s19, v135
	v_mov_b32_e32 v138, 0
	v_cvt_pk_fp8_f32 v138, v66, v67
	v_mul_f32_e32 v66, s31, v84
	v_mul_f32_e32 v67, s31, v80
	v_med3_f32 v66, v66, s19, v135
	v_med3_f32 v67, v67, s19, v135
	v_cvt_pk_fp8_f32 v138, v66, v67 op_sel:[0,0,1]
	v_mul_f32_e32 v66, s31, v76
	v_mul_f32_e32 v67, s31, v104
	v_med3_f32 v66, v66, s19, v135
	v_med3_f32 v67, v67, s19, v135
	v_mov_b32_e32 v139, 0
	v_cvt_pk_fp8_f32 v139, v66, v67
	v_mul_f32_e32 v66, s31, v92
	v_mul_f32_e32 v67, s31, v88
	v_med3_f32 v66, v66, s19, v135
	v_med3_f32 v67, v67, s19, v135
	v_cvt_pk_fp8_f32 v139, v66, v67 op_sel:[0,0,1]
	v_mul_f32_e32 v66, s31, v96
	v_mul_f32_e32 v67, s31, v100
	v_med3_f32 v66, v66, s19, v135
	v_med3_f32 v67, v67, s19, v135
	v_mov_b32_e32 v140, 0
	v_cvt_pk_fp8_f32 v140, v66, v67
	v_mul_f32_e32 v66, s31, v116
	v_mul_f32_e32 v67, s31, v108
	v_med3_f32 v66, v66, s19, v135
	v_med3_f32 v67, v67, s19, v135
	v_cvt_pk_fp8_f32 v140, v66, v67 op_sel:[0,0,1]
	v_mul_f32_e32 v66, s31, v112
	v_mul_f32_e32 v67, s31, v120
	v_med3_f32 v66, v66, s19, v135
	v_med3_f32 v67, v67, s19, v135
	v_mov_b32_e32 v141, 0
	v_cvt_pk_fp8_f32 v141, v66, v67
	v_mul_f32_e32 v66, s31, v124
	v_mul_f32_e32 v67, s31, v128
	v_med3_f32 v66, v66, s19, v135
	v_med3_f32 v67, v67, s19, v135
	v_cvt_pk_fp8_f32 v141, v66, v67 op_sel:[0,0,1]
	v_or_b32_e32 v66, 2, v130
	v_bitop3_b32 v67, v130, s21, 2 bitop3:0xc8
	v_add_u32_e32 v66, s30, v66
	v_or_b32_e32 v67, s2, v67
	v_cndmask_b32_e64 v66, v67, v66, s[4:5]
	v_ashrrev_i32_e32 v67, 31, v66
	v_mul_lo_u32 v68, s6, v67
	v_mul_lo_u32 v70, s7, v66
	v_mad_u64_u32 v[66:67], s[8:9], s6, v66, v[132:133]
	v_add3_u32 v67, v70, v67, v68
	global_store_dwordx4 v[66:67], v[138:141], off nt
	v_mul_f32_e32 v66, s31, v69
	v_mul_f32_e32 v67, s31, v73
	v_med3_f32 v69, v66, s19, v135
	v_med3_f32 v67, v67, s19, v135
	v_mov_b32_e32 v66, 0
	v_cvt_pk_fp8_f32 v66, v69, v67
	v_mul_f32_e32 v68, s31, v85
	v_mul_f32_e32 v67, s31, v81
	v_med3_f32 v68, v68, s19, v135
	v_med3_f32 v67, v67, s19, v135
	v_cvt_pk_fp8_f32 v66, v68, v67 op_sel:[0,0,1]
	v_mul_f32_e32 v67, s31, v77
	v_mul_f32_e32 v68, s31, v105
	v_med3_f32 v70, v67, s19, v135
	v_med3_f32 v68, v68, s19, v135
	v_mov_b32_e32 v67, 0
	v_cvt_pk_fp8_f32 v67, v70, v68
	v_mul_f32_e32 v69, s31, v93
	v_mul_f32_e32 v68, s31, v89
	v_med3_f32 v69, v69, s19, v135
	v_med3_f32 v68, v68, s19, v135
	v_cvt_pk_fp8_f32 v67, v69, v68 op_sel:[0,0,1]
	v_mul_f32_e32 v68, s31, v97
	v_mul_f32_e32 v69, s31, v101
	v_med3_f32 v71, v68, s19, v135
	v_med3_f32 v69, v69, s19, v135
	v_mov_b32_e32 v68, 0
	v_cvt_pk_fp8_f32 v68, v71, v69
	v_mul_f32_e32 v70, s31, v117
	v_mul_f32_e32 v69, s31, v109
	v_med3_f32 v70, v70, s19, v135
	v_med3_f32 v69, v69, s19, v135
	v_cvt_pk_fp8_f32 v68, v70, v69 op_sel:[0,0,1]
	v_mul_f32_e32 v69, s31, v113
	v_mul_f32_e32 v70, s31, v121
	v_med3_f32 v72, v69, s19, v135
	v_med3_f32 v70, v70, s19, v135
	v_mov_b32_e32 v69, 0
	v_cvt_pk_fp8_f32 v69, v72, v70
	v_mul_f32_e32 v71, s31, v125
	v_mul_f32_e32 v70, s31, v129
	v_med3_f32 v71, v71, s19, v135
	v_med3_f32 v70, v70, s19, v135
	v_cvt_pk_fp8_f32 v69, v71, v70 op_sel:[0,0,1]
	v_or_b32_e32 v70, 3, v130
	v_bitop3_b32 v71, v130, s22, 3 bitop3:0xc8
	v_add_u32_e32 v70, s30, v70
	v_or_b32_e32 v71, s2, v71
	v_cndmask_b32_e64 v72, v71, v70, s[4:5]
	v_ashrrev_i32_e32 v70, 31, v72
	v_mul_lo_u32 v73, s6, v70
	v_mad_u64_u32 v[70:71], s[8:9], s6, v72, v[132:133]
	v_mul_lo_u32 v72, s7, v72
	v_add3_u32 v71, v72, v71, v73
	s_waitcnt vmcnt(10)
; __device__ __forceinline__ unsigned pk4_fp8(float a, float b, float c, float d) { int w = 0; w = __builtin_amdgcn_cvt_pk_fp8_f32(clamp448(a), clamp448(b), w, false); w = __builtin_amdgcn_cvt_pk_fp8_f32(clamp448(c), clamp448(d), w, true); return (unsigned)w; }
; __device__ __forceinline__ void transpose_item_f8(const float* W, int N, unsigned char* WT, int ldt, int kind, int off, int item, int lane, float scale) {
;     ...
;     for (int hh = 0; hh < 2; ++hh)
; #pragma unroll
;         for (int i = 0; i < 4; ++i) { v4u o; o.x = pg8::pk4_fp8(v[hh][0][i] * scale, v[hh][1][i] * scale, v[hh][2][i] * scale, v[hh][3][i] * scale); o.y = pg8::pk4_fp8(v[hh][4][i] * scale, v[hh][5][i] * scale, v[hh][6][i] * scale, v[hh][7][i] * scale);
;             o.z = pg8::pk4_fp8(v[hh][8][i] * scale, v[hh][9][i] * scale, v[hh][10][i] * scale, v[hh][11][i] * scale); o.w = pg8::pk4_fp8(v[hh][12][i] * scale, v[hh][13][i] * scale, v[hh][14][i] * scale, v[hh][15][i] * scale);
;             __builtin_nontemporal_store(o, (v4u*)(WT + (size_t)rowmap(kind, off, n + 32 * hh + i) * ldt + k0)); }
	v_mul_f32_e32 v10, s31, v10
	s_waitcnt vmcnt(9)
	v_mul_f32_e32 v14, s31, v14
	global_store_dwordx4 v[70:71], v[66:69], off nt
	v_med3_f32 v10, v10, s19, v135
	v_med3_f32 v14, v14, s19, v135
	v_mov_b32_e32 v68, 0
	v_cvt_pk_fp8_f32 v68, v10, v14
	s_waitcnt vmcnt(9)
	v_mul_f32_e32 v18, s31, v18
	s_waitcnt vmcnt(8)
	v_mul_f32_e32 v6, s31, v6
	v_med3_f32 v10, v18, s19, v135
	v_med3_f32 v6, v6, s19, v135
	v_cvt_pk_fp8_f32 v68, v10, v6 op_sel:[0,0,1]
	s_waitcnt vmcnt(7)
	v_mul_f32_e32 v2, s31, v2
	s_waitcnt vmcnt(6)
	v_mul_f32_e32 v6, s31, v54
	v_med3_f32 v2, v2, s19, v135
	v_med3_f32 v6, v6, s19, v135
	v_mov_b32_e32 v69, 0
	v_mul_f32_e32 v42, s31, v42
	v_mul_f32_e32 v46, s31, v46
	v_mul_f32_e32 v30, s31, v30
	v_mul_f32_e32 v34, s31, v34
	v_cvt_pk_fp8_f32 v69, v2, v6
	v_med3_f32 v42, v42, s19, v135
	v_med3_f32 v46, v46, s19, v135
	v_mov_b32_e32 v66, 0
	v_med3_f32 v30, v30, s19, v135
	v_med3_f32 v34, v34, s19, v135
	v_mov_b32_e32 v67, 0
	v_cvt_pk_fp8_f32 v66, v42, v46
	v_cvt_pk_fp8_f32 v67, v30, v34
	s_waitcnt vmcnt(5)
	v_mul_f32_e32 v10, s31, v62
	s_waitcnt vmcnt(4)
	v_mul_f32_e32 v2, s31, v58
	v_med3_f32 v6, v10, s19, v135
	v_med3_f32 v2, v2, s19, v135
	v_or_b32_e32 v70, 32, v130
	v_mul_f32_e32 v50, s31, v50
	v_mul_f32_e32 v38, s31, v38
	v_mul_f32_e32 v26, s31, v26
	v_mul_f32_e32 v22, s31, v22
	v_cvt_pk_fp8_f32 v69, v6, v2 op_sel:[0,0,1]
	v_bitop3_b32 v6, v130, s23, 32 bitop3:0xc8
	v_med3_f32 v42, v50, s19, v135
	v_med3_f32 v38, v38, s19, v135
	v_med3_f32 v26, v26, s19, v135
	v_med3_f32 v22, v22, s19, v135
	v_add_u32_e32 v2, s30, v70
	v_or_b32_e32 v6, s2, v6
	v_cvt_pk_fp8_f32 v66, v42, v38 op_sel:[0,0,1]
	v_cvt_pk_fp8_f32 v67, v26, v22 op_sel:[0,0,1]
	v_cndmask_b32_e64 v2, v6, v2, s[4:5]
	v_ashrrev_i32_e32 v6, 31, v2
	v_mul_lo_u32 v6, s6, v6
	v_mad_u64_u32 v[70:71], s[8:9], s6, v2, v[132:133]
	v_mul_lo_u32 v2, s7, v2
	v_add3_u32 v71, v2, v71, v6
	v_mul_f32_e32 v2, s31, v43
	v_mul_f32_e32 v6, s31, v47
	global_store_dwordx4 v[70:71], v[66:69], off nt
	v_med3_f32 v2, v2, s19, v135
	v_med3_f32 v6, v6, s19, v135
	v_mov_b32_e32 v66, 0
	v_cvt_pk_fp8_f32 v66, v2, v6
	v_mul_f32_e32 v10, s31, v51
	v_mul_f32_e32 v2, s31, v39
	v_med3_f32 v6, v10, s19, v135
	v_med3_f32 v2, v2, s19, v135
	v_cvt_pk_fp8_f32 v66, v6, v2 op_sel:[0,0,1]
	v_mul_f32_e32 v2, s31, v31
	v_mul_f32_e32 v6, s31, v35
	v_med3_f32 v2, v2, s19, v135
	v_med3_f32 v6, v6, s19, v135
	v_mov_b32_e32 v67, 0
	v_cvt_pk_fp8_f32 v67, v2, v6
	v_mul_f32_e32 v10, s31, v27
	v_mul_f32_e32 v2, s31, v23
	v_med3_f32 v6, v10, s19, v135
	v_med3_f32 v2, v2, s19, v135
	v_cvt_pk_fp8_f32 v67, v6, v2 op_sel:[0,0,1]
	v_mul_f32_e32 v2, s31, v11
	v_mul_f32_e32 v6, s31, v15
	v_med3_f32 v2, v2, s19, v135
	v_med3_f32 v6, v6, s19, v135
	v_mov_b32_e32 v68, 0
	v_cvt_pk_fp8_f32 v68, v2, v6
	v_mul_f32_e32 v10, s31, v19
	v_mul_f32_e32 v2, s31, v7
	v_med3_f32 v6, v10, s19, v135
	v_med3_f32 v2, v2, s19, v135
	v_cvt_pk_fp8_f32 v68, v6, v2 op_sel:[0,0,1]
	v_mul_f32_e32 v2, s31, v3
	v_mul_f32_e32 v3, s31, v55
	v_med3_f32 v2, v2, s19, v135
	v_med3_f32 v3, v3, s19, v135
	v_mov_b32_e32 v69, 0
	v_cvt_pk_fp8_f32 v69, v2, v3
	v_mul_f32_e32 v6, s31, v63
	v_mul_f32_e32 v2, s31, v59
	v_med3_f32 v3, v6, s19, v135
	v_med3_f32 v2, v2, s19, v135
	v_cvt_pk_fp8_f32 v69, v3, v2 op_sel:[0,0,1]
	v_or_b32_e32 v2, 33, v130
	v_bitop3_b32 v3, v130, s26, 33 bitop3:0xc8
	v_add_u32_e32 v2, s30, v2
	v_or_b32_e32 v3, s2, v3
	v_cndmask_b32_e64 v6, v3, v2, s[4:5]
	v_ashrrev_i32_e32 v2, 31, v6
	v_mul_lo_u32 v7, s6, v2
	v_mad_u64_u32 v[2:3], s[8:9], s6, v6, v[132:133]
	v_mul_lo_u32 v6, s7, v6
	v_add3_u32 v3, v6, v3, v7
	global_store_dwordx4 v[2:3], v[66:69], off nt
	v_mul_f32_e32 v2, s31, v44
	v_mul_f32_e32 v3, s31, v48
	v_med3_f32 v2, v2, s19, v135
	v_med3_f32 v3, v3, s19, v135
	v_mov_b32_e32 v66, 0
	v_cvt_pk_fp8_f32 v66, v2, v3
	v_mul_f32_e32 v6, s31, v52
	v_mul_f32_e32 v2, s31, v40
	v_med3_f32 v3, v6, s19, v135
	v_med3_f32 v2, v2, s19, v135
	v_cvt_pk_fp8_f32 v66, v3, v2 op_sel:[0,0,1]
	v_mul_f32_e32 v2, s31, v32
	v_mul_f32_e32 v3, s31, v36
	v_med3_f32 v2, v2, s19, v135
	v_med3_f32 v3, v3, s19, v135
	v_mov_b32_e32 v67, 0
	v_cvt_pk_fp8_f32 v67, v2, v3
	v_mul_f32_e32 v6, s31, v28
	v_mul_f32_e32 v2, s31, v24
	v_med3_f32 v3, v6, s19, v135
	v_med3_f32 v2, v2, s19, v135
	v_cvt_pk_fp8_f32 v67, v3, v2 op_sel:[0,0,1]
	v_mul_f32_e32 v2, s31, v12
	v_mul_f32_e32 v3, s31, v16
	v_med3_f32 v2, v2, s19, v135
	v_med3_f32 v3, v3, s19, v135
	v_mov_b32_e32 v68, 0
	v_cvt_pk_fp8_f32 v68, v2, v3
	v_mul_f32_e32 v6, s31, v20
	v_mul_f32_e32 v2, s31, v8
	v_med3_f32 v3, v6, s19, v135
	v_med3_f32 v2, v2, s19, v135
	v_cvt_pk_fp8_f32 v68, v3, v2 op_sel:[0,0,1]
	v_mul_f32_e32 v2, s31, v4
	v_mul_f32_e32 v3, s31, v56
	v_med3_f32 v2, v2, s19, v135
	v_med3_f32 v3, v3, s19, v135
	v_mov_b32_e32 v69, 0
	v_cvt_pk_fp8_f32 v69, v2, v3
	v_mul_f32_e32 v4, s31, v64
	v_mul_f32_e32 v2, s31, v60
	v_med3_f32 v3, v4, s19, v135
	v_med3_f32 v2, v2, s19, v135
	v_cvt_pk_fp8_f32 v69, v3, v2 op_sel:[0,0,1]
	v_or_b32_e32 v2, 34, v130
	v_bitop3_b32 v3, v130, s27, 34 bitop3:0xc8
	v_add_u32_e32 v2, s30, v2
	v_or_b32_e32 v3, s2, v3
	v_cndmask_b32_e64 v4, v3, v2, s[4:5]
	v_ashrrev_i32_e32 v2, 31, v4
	v_mul_lo_u32 v6, s6, v2
	v_mad_u64_u32 v[2:3], s[8:9], s6, v4, v[132:133]
	v_mul_lo_u32 v4, s7, v4
	v_add3_u32 v3, v4, v3, v6
	global_store_dwordx4 v[2:3], v[66:69], off nt
	v_mul_f32_e32 v2, s31, v45
	v_mul_f32_e32 v3, s31, v49
	v_med3_f32 v6, v2, s19, v135
	v_med3_f32 v3, v3, s19, v135
	v_mov_b32_e32 v2, 0
	v_cvt_pk_fp8_f32 v2, v6, v3
	v_mul_f32_e32 v4, s31, v53
	v_mul_f32_e32 v3, s31, v41
	v_med3_f32 v4, v4, s19, v135
	v_med3_f32 v3, v3, s19, v135
	v_cvt_pk_fp8_f32 v2, v4, v3 op_sel:[0,0,1]
	v_mul_f32_e32 v3, s31, v33
	v_mul_f32_e32 v4, s31, v37
	v_med3_f32 v7, v3, s19, v135
	v_med3_f32 v4, v4, s19, v135
	v_mov_b32_e32 v3, 0
	v_cvt_pk_fp8_f32 v3, v7, v4
	v_mul_f32_e32 v6, s31, v29
	v_mul_f32_e32 v4, s31, v25
	v_med3_f32 v6, v6, s19, v135
	v_med3_f32 v4, v4, s19, v135
	v_cvt_pk_fp8_f32 v3, v6, v4 op_sel:[0,0,1]
	v_mul_f32_e32 v4, s31, v13
	v_mul_f32_e32 v6, s31, v17
	v_med3_f32 v8, v4, s19, v135
	v_med3_f32 v6, v6, s19, v135
	v_mov_b32_e32 v4, 0
	v_cvt_pk_fp8_f32 v4, v8, v6
	v_mul_f32_e32 v7, s31, v21
	v_mul_f32_e32 v6, s31, v9
	v_med3_f32 v7, v7, s19, v135
	v_med3_f32 v6, v6, s19, v135
	v_cvt_pk_fp8_f32 v4, v7, v6 op_sel:[0,0,1]
	v_mul_f32_e32 v5, s31, v5
	v_mul_f32_e32 v6, s31, v57
	v_med3_f32 v8, v5, s19, v135
	v_med3_f32 v6, v6, s19, v135
	v_mov_b32_e32 v5, 0
	v_cvt_pk_fp8_f32 v5, v8, v6
	v_mul_f32_e32 v7, s31, v65
	v_mul_f32_e32 v6, s31, v61
	v_med3_f32 v7, v7, s19, v135
	v_med3_f32 v6, v6, s19, v135
	v_cvt_pk_fp8_f32 v5, v7, v6 op_sel:[0,0,1]
	v_or_b32_e32 v6, 35, v130
	v_bitop3_b32 v7, v130, s28, 35 bitop3:0xc8
	v_add_u32_e32 v6, s30, v6
	v_or_b32_e32 v7, s2, v7
	v_cndmask_b32_e64 v8, v7, v6, s[4:5]
	v_ashrrev_i32_e32 v6, 31, v8
	v_mul_lo_u32 v9, s6, v6
	v_mad_u64_u32 v[6:7], s[4:5], s6, v8, v[132:133]
	v_mul_lo_u32 v8, s7, v8
	v_add3_u32 v7, v8, v7, v9
	global_store_dwordx4 v[6:7], v[2:5], off nt
	s_cbranch_scc0 .LBB0_246

; __device__ __forceinline__ void moe_convert(Frame& F, int lo, int hi, int rank, int nrank) {
;     if (MOE_DMA) { moe_convert_dma(F, lo, hi, rank, nrank); return; }
;     for (int it = lo + rank; it < hi; it += nrank) {
;         int r = it; const float* W; unsigned char* WT; int N, ldt, kind, off; float f8s;
;         if (r < 14336) { const int e = r / 1792; r -= e * 1792; W = F.in[IN_WMG] + (size_t)e * 2048 * DFFE; N = DFFE; WT = F.ws + WS_WGU1 + (size_t)e * 14336 * 2048; ldt = 2048; kind = 1; off = 0; f8s = 32.f; }
;         else if ((r -= 14336) < 14336) { const int e = r / 1792; r -= e * 1792; W = F.in[IN_WMU] + (size_t)e * 2048 * DFFE; N = DFFE; WT = F.ws + WS_WGU1 + (size_t)e * 14336 * 2048; ldt = 2048; kind = 1; off = 128; f8s = 256.f; }
;         else { r -= 14336; const int e = r / 1792; r -= e * 1792; W = F.in[IN_WMD] + (size_t)e * DFFE * 2048; N = 2048; WT = F.ws + WS_WDN1 + (size_t)e * 2048 * DFFE; ldt = DFFE; kind = 0; off = 0; f8s = 64.f; }
;         transpose_item_f8(W, N, WT, ldt, kind, off, r, F.lane, f8s);
.Lsf0_notw0:
	s_cmp_gt_u32 s4, 3
	s_cbranch_scc1 .Lsf0_skip
	v_mov_b32_e32 v8, 0x20020
	ds_read_b32 v9, v8 offset:4
	v_mbcnt_lo_u32_b32 v2, -1, 0
	v_mbcnt_hi_u32_b32 v2, -1, v2
	s_waitcnt lgkmcnt(0)
	v_readfirstlane_b32 s5, v9
	s_cmp_ge_u32 s5, 48
	s_cbranch_scc1 .Lsf0_skip
	s_add_i32 s5, s4, -1
	s_lshl_b32 s5, s5, 14
	v_lshl_add_u32 v7, v2, 4, s5
	ds_write_b128 v7, v[160:163] offset:0
	ds_write_b128 v7, v[164:167] offset:1024
	ds_write_b128 v7, v[168:171] offset:2048
	ds_write_b128 v7, v[172:175] offset:3072
	ds_write_b128 v7, v[176:179] offset:4096
	ds_write_b128 v7, v[180:183] offset:5120
	ds_write_b128 v7, v[184:187] offset:6144
	ds_write_b128 v7, v[188:191] offset:7168
	ds_write_b128 v7, v[192:195] offset:8192
	ds_write_b128 v7, v[196:199] offset:9216
	ds_write_b128 v7, v[200:203] offset:10240
	ds_write_b128 v7, v[204:207] offset:11264
	ds_write_b128 v7, v[208:211] offset:12288
	ds_write_b128 v7, v[212:215] offset:13312
	ds_write_b128 v7, v[216:219] offset:14336
	ds_write_b128 v7, v[220:223] offset:15360
	v_readlane_b32 s6, v247, 0
	v_readlane_b32 s7, v247, 1
	s_load_dwordx2 s[10:11], s[6:7], 0xc0
	s_load_dwordx2 s[12:13], s[6:7], 0xc8
	v_readlane_b32 s33, v247, 6
	v_mov_b32_e32 v3, 0x43e00000
	v_cmp_eq_u32_e32 vcc, 0, v2
	s_mul_i32 s33, s33, 48
	s_nop 1
	v_cndmask_b32_e64 v18, 0, 1, vcc
	s_waitcnt lgkmcnt(0)
	s_mov_b32 s34, 1
.Lsf0_loop:
	ds_read_b32 v9, v8
	s_waitcnt lgkmcnt(0)
	v_readfirstlane_b32 s5, v9
	s_cmp_eq_u32 s5, 1
	s_cbranch_scc1 .Lsf0_done
	ds_add_rtn_u32 v9, v8, v18 offset:4
	s_waitcnt lgkmcnt(0)
	v_readfirstlane_b32 s18, v9
	s_cmp_ge_u32 s18, 48
	s_cbranch_scc1 .Lsf0_done
	s_add_i32 s18, s18, s33
	s_and_b32 s27, s18, 1
	s_lshr_b32 s19, s18, 1
	s_add_i32 s19, s19, 0x7000
	s_cmp_lt_u32 s19, 0x7000
	s_cbranch_scc0 .Lsf0_down
	s_add_i32 s20, s19, 0xffffc800
	s_lshr_b32 s21, s20, 8
	s_mul_i32 s21, s21, 37
	s_lshr_b32 s21, s21, 8
	s_mul_i32 s28, s21, 0x700
	s_sub_i32 s20, s20, s28
	s_mul_i32 s28, s21, 0x3800000
	s_add_u32 s14, s10, s28
	s_addc_u32 s15, s11, 0
	s_mul_i32 s28, s21, 0x1c00000
	s_add_u32 s28, s28, 0x7800000
	s_add_u32 s16, s86, s28
	s_addc_u32 s17, s87, 0
	s_movk_i32 s24, 0x7000
	s_movk_i32 s25, 0x800
	s_mov_b32 s26, 0x43800000
	s_lshr_b32 s22, s20, 4
	s_mul_i32 s22, s22, 0x2493
	s_lshr_b32 s22, s22, 16
	s_mul_i32 s28, s22, 0x70
	s_sub_i32 s23, s20, s28
	s_mov_b32 s29, 1
	s_branch .Lsf0_dec

; __device__ __forceinline__ void moe_convert(Frame& F, int lo, int hi, int rank, int nrank) {
;     ...
;     for (int it = lo + rank; it < hi; it += nrank) {
;         int r = it; const float* W; unsigned char* WT; int N, ldt, kind, off; float f8s;
;         if (r < 14336) { const int e = r / 1792; r -= e * 1792; W = F.in[IN_WMG] + (size_t)e * 2048 * DFFE; N = DFFE; WT = F.ws + WS_WGU1 + (size_t)e * 14336 * 2048; ldt = 2048; kind = 1; off = 0; f8s = 32.f; }
;         else if ((r -= 14336) < 14336) { const int e = r / 1792; r -= e * 1792; W = F.in[IN_WMU] + (size_t)e * 2048 * DFFE; N = DFFE; WT = F.ws + WS_WGU1 + (size_t)e * 14336 * 2048; ldt = 2048; kind = 1; off = 128; f8s = 256.f; }
;         else { r -= 14336; const int e = r / 1792; r -= e * 1792; W = F.in[IN_WMD] + (size_t)e * DFFE * 2048; N = 2048; WT = F.ws + WS_WDN1 + (size_t)e * 2048 * DFFE; ldt = DFFE; kind = 0; off = 0; f8s = 64.f; }
;         transpose_item_f8(W, N, WT, ldt, kind, off, r, F.lane, f8s);
.Lsf1_loop:
	ds_read_b32 v9, v8
	s_waitcnt lgkmcnt(0)
	v_readfirstlane_b32 s5, v9
	s_cmp_eq_u32 s5, 2
	s_cbranch_scc1 .Lsf1_done
	ds_add_rtn_u32 v9, v8, v18 offset:4
	s_waitcnt lgkmcnt(0)
	v_readfirstlane_b32 s18, v9
	s_cmp_ge_u32 s18, 48
	s_cbranch_scc1 .Lsf1_done
	s_add_i32 s18, s18, s33
	s_and_b32 s27, s18, 1
	s_lshr_b32 s19, s18, 1
	s_add_i32 s19, s19, 0x7000
	s_cmp_lt_u32 s19, 0x7000
	s_cbranch_scc0 .Lsf1_down
	s_add_i32 s20, s19, 0xffffc800
	s_lshr_b32 s21, s20, 8
	s_mul_i32 s21, s21, 37
	s_lshr_b32 s21, s21, 8
	s_mul_i32 s28, s21, 0x700
	s_sub_i32 s20, s20, s28
	s_mul_i32 s28, s21, 0x3800000
	s_add_u32 s14, s10, s28
	s_addc_u32 s15, s11, 0
	s_mul_i32 s28, s21, 0x1c00000
	s_add_u32 s28, s28, 0x7800000
	s_add_u32 s16, s86, s28
	s_addc_u32 s17, s87, 0
	s_movk_i32 s24, 0x7000
	s_movk_i32 s25, 0x800
	s_mov_b32 s26, 0x43800000
	s_lshr_b32 s22, s20, 4
	s_mul_i32 s22, s22, 0x2493
	s_lshr_b32 s22, s22, 16
	s_mul_i32 s28, s22, 0x70
	s_sub_i32 s23, s20, s28
	s_mov_b32 s29, 1
	s_branch .Lsf1_dec

; __device__ __forceinline__ void moe_convert(Frame& F, int lo, int hi, int rank, int nrank) {
;     ...
;     for (int it = lo + rank; it < hi; it += nrank) {
;         int r = it; const float* W; unsigned char* WT; int N, ldt, kind, off; float f8s;
;         if (r < 14336) { const int e = r / 1792; r -= e * 1792; W = F.in[IN_WMG] + (size_t)e * 2048 * DFFE; N = DFFE; WT = F.ws + WS_WGU1 + (size_t)e * 14336 * 2048; ldt = 2048; kind = 1; off = 0; f8s = 32.f; }
;         else if ((r -= 14336) < 14336) { const int e = r / 1792; r -= e * 1792; W = F.in[IN_WMU] + (size_t)e * 2048 * DFFE; N = DFFE; WT = F.ws + WS_WGU1 + (size_t)e * 14336 * 2048; ldt = 2048; kind = 1; off = 128; f8s = 256.f; }
;         else { r -= 14336; const int e = r / 1792; r -= e * 1792; W = F.in[IN_WMD] + (size_t)e * DFFE * 2048; N = 2048; WT = F.ws + WS_WDN1 + (size_t)e * 2048 * DFFE; ldt = DFFE; kind = 0; off = 0; f8s = 64.f; }
;         transpose_item_f8(W, N, WT, ldt, kind, off, r, F.lane, f8s);
.Lsf2_loop:
	ds_read_b32 v9, v8
	s_waitcnt lgkmcnt(0)
	v_readfirstlane_b32 s5, v9
	s_cmp_eq_u32 s5, 3
	s_cbranch_scc1 .Lsf2_done
	ds_add_rtn_u32 v9, v8, v18 offset:4
	s_waitcnt lgkmcnt(0)
	v_readfirstlane_b32 s18, v9
	s_cmp_ge_u32 s18, 48
	s_cbranch_scc1 .Lsf2_done
	s_add_i32 s18, s18, s33
	s_and_b32 s27, s18, 1
	s_lshr_b32 s19, s18, 1
	s_add_i32 s19, s19, 0x7000
	s_cmp_lt_u32 s19, 0x7000
	s_cbranch_scc0 .Lsf2_down
	s_add_i32 s20, s19, 0xffffc800
	s_lshr_b32 s21, s20, 8
	s_mul_i32 s21, s21, 37
	s_lshr_b32 s21, s21, 8
	s_mul_i32 s28, s21, 0x700
	s_sub_i32 s20, s20, s28
	s_mul_i32 s28, s21, 0x3800000
	s_add_u32 s14, s10, s28
	s_addc_u32 s15, s11, 0
	s_mul_i32 s28, s21, 0x1c00000
	s_add_u32 s28, s28, 0x7800000
	s_add_u32 s16, s86, s28
	s_addc_u32 s17, s87, 0
	s_movk_i32 s24, 0x7000
	s_movk_i32 s25, 0x800
	s_mov_b32 s26, 0x43800000
	s_lshr_b32 s22, s20, 4
	s_mul_i32 s22, s22, 0x2493
	s_lshr_b32 s22, s22, 16
	s_mul_i32 s28, s22, 0x70
	s_sub_i32 s23, s20, s28
	s_mov_b32 s29, 1
	s_branch .Lsf2_dec

; __device__ __forceinline__ void moe_convert(Frame& F, int lo, int hi, int rank, int nrank) {
;     ...
;     for (int it = lo + rank; it < hi; it += nrank) {
;         int r = it; const float* W; unsigned char* WT; int N, ldt, kind, off; float f8s;
;         if (r < 14336) { const int e = r / 1792; r -= e * 1792; W = F.in[IN_WMG] + (size_t)e * 2048 * DFFE; N = DFFE; WT = F.ws + WS_WGU1 + (size_t)e * 14336 * 2048; ldt = 2048; kind = 1; off = 0; f8s = 32.f; }
;         else if ((r -= 14336) < 14336) { const int e = r / 1792; r -= e * 1792; W = F.in[IN_WMU] + (size_t)e * 2048 * DFFE; N = DFFE; WT = F.ws + WS_WGU1 + (size_t)e * 14336 * 2048; ldt = 2048; kind = 1; off = 128; f8s = 256.f; }
;         else { r -= 14336; const int e = r / 1792; r -= e * 1792; W = F.in[IN_WMD] + (size_t)e * DFFE * 2048; N = 2048; WT = F.ws + WS_WDN1 + (size_t)e * 2048 * DFFE; ldt = DFFE; kind = 0; off = 0; f8s = 64.f; }
;         transpose_item_f8(W, N, WT, ldt, kind, off, r, F.lane, f8s);
.Lsf3_loop:
	ds_read_b32 v9, v8
	s_waitcnt lgkmcnt(0)
	v_readfirstlane_b32 s5, v9
	s_cmp_eq_u32 s5, 4
	s_cbranch_scc1 .Lsf3_done
	ds_add_rtn_u32 v9, v8, v18 offset:4
	s_waitcnt lgkmcnt(0)
	v_readfirstlane_b32 s18, v9
	s_cmp_ge_u32 s18, 48
	s_cbranch_scc1 .Lsf3_done
	s_add_i32 s18, s18, s33
	s_and_b32 s27, s18, 1
	s_lshr_b32 s19, s18, 1
	s_add_i32 s19, s19, 0x7000
	s_cmp_lt_u32 s19, 0x7000
	s_cbranch_scc0 .Lsf3_down
	s_add_i32 s20, s19, 0xffffc800
	s_lshr_b32 s21, s20, 8
	s_mul_i32 s21, s21, 37
	s_lshr_b32 s21, s21, 8
	s_mul_i32 s28, s21, 0x700
	s_sub_i32 s20, s20, s28
	s_mul_i32 s28, s21, 0x3800000
	s_add_u32 s14, s10, s28
	s_addc_u32 s15, s11, 0
	s_mul_i32 s28, s21, 0x1c00000
	s_add_u32 s28, s28, 0x7800000
	s_add_u32 s16, s86, s28
	s_addc_u32 s17, s87, 0
	s_movk_i32 s24, 0x7000
	s_movk_i32 s25, 0x800
	s_mov_b32 s26, 0x43800000
	s_lshr_b32 s22, s20, 4
	s_mul_i32 s22, s22, 0x2493
	s_lshr_b32 s22, s22, 16
	s_mul_i32 s28, s22, 0x70
	s_sub_i32 s23, s20, s28
	s_mov_b32 s29, 1
	s_branch .Lsf3_dec

; __device__ __forceinline__ void moe_convert(Frame& F, int lo, int hi, int rank, int nrank) {
;     ...
;     for (int it = lo + rank; it < hi; it += nrank) {
;         int r = it; const float* W; unsigned char* WT; int N, ldt, kind, off; float f8s;
;         if (r < 14336) { const int e = r / 1792; r -= e * 1792; W = F.in[IN_WMG] + (size_t)e * 2048 * DFFE; N = DFFE; WT = F.ws + WS_WGU1 + (size_t)e * 14336 * 2048; ldt = 2048; kind = 1; off = 0; f8s = 32.f; }
;         else if ((r -= 14336) < 14336) { const int e = r / 1792; r -= e * 1792; W = F.in[IN_WMU] + (size_t)e * 2048 * DFFE; N = DFFE; WT = F.ws + WS_WGU1 + (size_t)e * 14336 * 2048; ldt = 2048; kind = 1; off = 128; f8s = 256.f; }
;         else { r -= 14336; const int e = r / 1792; r -= e * 1792; W = F.in[IN_WMD] + (size_t)e * DFFE * 2048; N = 2048; WT = F.ws + WS_WDN1 + (size_t)e * 2048 * DFFE; ldt = DFFE; kind = 0; off = 0; f8s = 64.f; }
;         transpose_item_f8(W, N, WT, ldt, kind, off, r, F.lane, f8s);
.Lsf4_loop:
	ds_read_b32 v9, v8
	s_waitcnt lgkmcnt(0)
	v_readfirstlane_b32 s5, v9
	s_cmp_eq_u32 s5, 5
	s_cbranch_scc1 .Lsf4_done
	ds_add_rtn_u32 v9, v8, v18 offset:4
	s_waitcnt lgkmcnt(0)
	v_readfirstlane_b32 s18, v9
	s_cmp_ge_u32 s18, 48
	s_cbranch_scc1 .Lsf4_done
	s_add_i32 s18, s18, s33
	s_and_b32 s27, s18, 1
	s_lshr_b32 s19, s18, 1
	s_add_i32 s19, s19, 0x7000
	s_cmp_lt_u32 s19, 0x7000
	s_cbranch_scc0 .Lsf4_down
	s_add_i32 s20, s19, 0xffffc800
	s_lshr_b32 s21, s20, 8
	s_mul_i32 s21, s21, 37
	s_lshr_b32 s21, s21, 8
	s_mul_i32 s28, s21, 0x700
	s_sub_i32 s20, s20, s28
	s_mul_i32 s28, s21, 0x3800000
	s_add_u32 s14, s10, s28
	s_addc_u32 s15, s11, 0
	s_mul_i32 s28, s21, 0x1c00000
	s_add_u32 s28, s28, 0x7800000
	s_add_u32 s16, s86, s28
	s_addc_u32 s17, s87, 0
	s_movk_i32 s24, 0x7000
	s_movk_i32 s25, 0x800
	s_mov_b32 s26, 0x43800000
	s_lshr_b32 s22, s20, 4
	s_mul_i32 s22, s22, 0x2493
	s_lshr_b32 s22, s22, 16
	s_mul_i32 s28, s22, 0x70
	s_sub_i32 s23, s20, s28
	s_mov_b32 s29, 1
	s_branch .Lsf4_dec

; __device__ __forceinline__ void moe_convert(Frame& F, int lo, int hi, int rank, int nrank) {
;     ...
;     for (int it = lo + rank; it < hi; it += nrank) {
;         int r = it; const float* W; unsigned char* WT; int N, ldt, kind, off; float f8s;
;         if (r < 14336) { const int e = r / 1792; r -= e * 1792; W = F.in[IN_WMG] + (size_t)e * 2048 * DFFE; N = DFFE; WT = F.ws + WS_WGU1 + (size_t)e * 14336 * 2048; ldt = 2048; kind = 1; off = 0; f8s = 32.f; }
;         else if ((r -= 14336) < 14336) { const int e = r / 1792; r -= e * 1792; W = F.in[IN_WMU] + (size_t)e * 2048 * DFFE; N = DFFE; WT = F.ws + WS_WGU1 + (size_t)e * 14336 * 2048; ldt = 2048; kind = 1; off = 128; f8s = 256.f; }
;         else { r -= 14336; const int e = r / 1792; r -= e * 1792; W = F.in[IN_WMD] + (size_t)e * DFFE * 2048; N = 2048; WT = F.ws + WS_WDN1 + (size_t)e * 2048 * DFFE; ldt = DFFE; kind = 0; off = 0; f8s = 64.f; }
;         transpose_item_f8(W, N, WT, ldt, kind, off, r, F.lane, f8s);
.Lsf5_loop:
	ds_read_b32 v9, v8
	s_waitcnt lgkmcnt(0)
	v_readfirstlane_b32 s5, v9
	s_cmp_eq_u32 s5, 6
	s_cbranch_scc1 .Lsf5_done
	ds_add_rtn_u32 v9, v8, v18 offset:4
	s_waitcnt lgkmcnt(0)
	v_readfirstlane_b32 s18, v9
	s_cmp_ge_u32 s18, 48
	s_cbranch_scc1 .Lsf5_done
	s_add_i32 s18, s18, s33
	s_and_b32 s27, s18, 1
	s_lshr_b32 s19, s18, 1
	s_add_i32 s19, s19, 0x7000
	s_cmp_lt_u32 s19, 0x7000
	s_cbranch_scc0 .Lsf5_down
	s_add_i32 s20, s19, 0xffffc800
	s_lshr_b32 s21, s20, 8
	s_mul_i32 s21, s21, 37
	s_lshr_b32 s21, s21, 8
	s_mul_i32 s28, s21, 0x700
	s_sub_i32 s20, s20, s28
	s_mul_i32 s28, s21, 0x3800000
	s_add_u32 s14, s10, s28
	s_addc_u32 s15, s11, 0
	s_mul_i32 s28, s21, 0x1c00000
	s_add_u32 s28, s28, 0x7800000
	s_add_u32 s16, s86, s28
	s_addc_u32 s17, s87, 0
	s_movk_i32 s24, 0x7000
	s_movk_i32 s25, 0x800
	s_mov_b32 s26, 0x43800000
	s_lshr_b32 s22, s20, 4
	s_mul_i32 s22, s22, 0x2493
	s_lshr_b32 s22, s22, 16
	s_mul_i32 s28, s22, 0x70
	s_sub_i32 s23, s20, s28
	s_mov_b32 s29, 1
	s_branch .Lsf5_dec

; __device__ __forceinline__ void moe_convert(Frame& F, int lo, int hi, int rank, int nrank) {
;     ...
;     for (int it = lo + rank; it < hi; it += nrank) {
;         int r = it; const float* W; unsigned char* WT; int N, ldt, kind, off; float f8s;
;         if (r < 14336) { const int e = r / 1792; r -= e * 1792; W = F.in[IN_WMG] + (size_t)e * 2048 * DFFE; N = DFFE; WT = F.ws + WS_WGU1 + (size_t)e * 14336 * 2048; ldt = 2048; kind = 1; off = 0; f8s = 32.f; }
;         else if ((r -= 14336) < 14336) { const int e = r / 1792; r -= e * 1792; W = F.in[IN_WMU] + (size_t)e * 2048 * DFFE; N = DFFE; WT = F.ws + WS_WGU1 + (size_t)e * 14336 * 2048; ldt = 2048; kind = 1; off = 128; f8s = 256.f; }
;         else { r -= 14336; const int e = r / 1792; r -= e * 1792; W = F.in[IN_WMD] + (size_t)e * DFFE * 2048; N = 2048; WT = F.ws + WS_WDN1 + (size_t)e * 2048 * DFFE; ldt = DFFE; kind = 0; off = 0; f8s = 64.f; }
;         transpose_item_f8(W, N, WT, ldt, kind, off, r, F.lane, f8s);
.Lsf6_loop:
	ds_read_b32 v9, v8
	s_waitcnt lgkmcnt(0)
	v_readfirstlane_b32 s5, v9
	s_cmp_eq_u32 s5, 7
	s_cbranch_scc1 .Lsf6_done
	ds_add_rtn_u32 v9, v8, v18 offset:4
	s_waitcnt lgkmcnt(0)
	v_readfirstlane_b32 s18, v9
	s_cmp_ge_u32 s18, 48
	s_cbranch_scc1 .Lsf6_done
	s_add_i32 s18, s18, s33
	s_and_b32 s27, s18, 1
	s_lshr_b32 s19, s18, 1
	s_add_i32 s19, s19, 0x7000
	s_cmp_lt_u32 s19, 0x7000
	s_cbranch_scc0 .Lsf6_down
	s_add_i32 s20, s19, 0xffffc800
	s_lshr_b32 s21, s20, 8
	s_mul_i32 s21, s21, 37
	s_lshr_b32 s21, s21, 8
	s_mul_i32 s28, s21, 0x700
	s_sub_i32 s20, s20, s28
	s_mul_i32 s28, s21, 0x3800000
	s_add_u32 s14, s10, s28
	s_addc_u32 s15, s11, 0
	s_mul_i32 s28, s21, 0x1c00000
	s_add_u32 s28, s28, 0x7800000
	s_add_u32 s16, s86, s28
	s_addc_u32 s17, s87, 0
	s_movk_i32 s24, 0x7000
	s_movk_i32 s25, 0x800
	s_mov_b32 s26, 0x43800000
	s_lshr_b32 s22, s20, 4
	s_mul_i32 s22, s22, 0x2493
	s_lshr_b32 s22, s22, 16
	s_mul_i32 s28, s22, 0x70
	s_sub_i32 s23, s20, s28
	s_mov_b32 s29, 1
	s_branch .Lsf6_dec

; __device__ __forceinline__ void moe_convert(Frame& F, int lo, int hi, int rank, int nrank) {
;     ...
;     for (int it = lo + rank; it < hi; it += nrank) {
;         int r = it; const float* W; unsigned char* WT; int N, ldt, kind, off; float f8s;
;         if (r < 14336) { const int e = r / 1792; r -= e * 1792; W = F.in[IN_WMG] + (size_t)e * 2048 * DFFE; N = DFFE; WT = F.ws + WS_WGU1 + (size_t)e * 14336 * 2048; ldt = 2048; kind = 1; off = 0; f8s = 32.f; }
;         else if ((r -= 14336) < 14336) { const int e = r / 1792; r -= e * 1792; W = F.in[IN_WMU] + (size_t)e * 2048 * DFFE; N = DFFE; WT = F.ws + WS_WGU1 + (size_t)e * 14336 * 2048; ldt = 2048; kind = 1; off = 128; f8s = 256.f; }
;         else { r -= 14336; const int e = r / 1792; r -= e * 1792; W = F.in[IN_WMD] + (size_t)e * DFFE * 2048; N = 2048; WT = F.ws + WS_WDN1 + (size_t)e * 2048 * DFFE; ldt = DFFE; kind = 0; off = 0; f8s = 64.f; }
;         transpose_item_f8(W, N, WT, ldt, kind, off, r, F.lane, f8s);
.Lsf7_loop:
	ds_read_b32 v9, v8
	s_waitcnt lgkmcnt(0)
	v_readfirstlane_b32 s5, v9
	s_cmp_eq_u32 s5, 8
	s_cbranch_scc1 .Lsf7_done
	ds_add_rtn_u32 v9, v8, v18 offset:4
	s_waitcnt lgkmcnt(0)
	v_readfirstlane_b32 s18, v9
	s_cmp_ge_u32 s18, 48
	s_cbranch_scc1 .Lsf7_done
	s_add_i32 s18, s18, s33
	s_and_b32 s27, s18, 1
	s_lshr_b32 s19, s18, 1
	s_add_i32 s19, s19, 0x7000
	s_cmp_lt_u32 s19, 0x7000
	s_cbranch_scc0 .Lsf7_down
	s_add_i32 s20, s19, 0xffffc800
	s_lshr_b32 s21, s20, 8
	s_mul_i32 s21, s21, 37
	s_lshr_b32 s21, s21, 8
	s_mul_i32 s28, s21, 0x700
	s_sub_i32 s20, s20, s28
	s_mul_i32 s28, s21, 0x3800000
	s_add_u32 s14, s10, s28
	s_addc_u32 s15, s11, 0
	s_mul_i32 s28, s21, 0x1c00000
	s_add_u32 s28, s28, 0x7800000
	s_add_u32 s16, s86, s28
	s_addc_u32 s17, s87, 0
	s_movk_i32 s24, 0x7000
	s_movk_i32 s25, 0x800
	s_mov_b32 s26, 0x43800000
	s_lshr_b32 s22, s20, 4
	s_mul_i32 s22, s22, 0x2493
	s_lshr_b32 s22, s22, 16
	s_mul_i32 s28, s22, 0x70
	s_sub_i32 s23, s20, s28
	s_mov_b32 s29, 1
	s_branch .Lsf7_dec

; __device__ __forceinline__ void moe_convert(Frame& F, int lo, int hi, int rank, int nrank) {
;     ...
;     for (int it = lo + rank; it < hi; it += nrank) {
;         int r = it; const float* W; unsigned char* WT; int N, ldt, kind, off; float f8s;
;         if (r < 14336) { const int e = r / 1792; r -= e * 1792; W = F.in[IN_WMG] + (size_t)e * 2048 * DFFE; N = DFFE; WT = F.ws + WS_WGU1 + (size_t)e * 14336 * 2048; ldt = 2048; kind = 1; off = 0; f8s = 32.f; }
;         else if ((r -= 14336) < 14336) { const int e = r / 1792; r -= e * 1792; W = F.in[IN_WMU] + (size_t)e * 2048 * DFFE; N = DFFE; WT = F.ws + WS_WGU1 + (size_t)e * 14336 * 2048; ldt = 2048; kind = 1; off = 128; f8s = 256.f; }
;         else { r -= 14336; const int e = r / 1792; r -= e * 1792; W = F.in[IN_WMD] + (size_t)e * DFFE * 2048; N = 2048; WT = F.ws + WS_WDN1 + (size_t)e * 2048 * DFFE; ldt = DFFE; kind = 0; off = 0; f8s = 64.f; }
;         transpose_item_f8(W, N, WT, ldt, kind, off, r, F.lane, f8s);
.Lsf8_loop:
	ds_read_b32 v9, v8
	s_waitcnt lgkmcnt(0)
	v_readfirstlane_b32 s5, v9
	s_cmp_eq_u32 s5, 9
	s_cbranch_scc1 .Lsf8_done
	ds_add_rtn_u32 v9, v8, v18 offset:4
	s_waitcnt lgkmcnt(0)
	v_readfirstlane_b32 s18, v9
	s_cmp_ge_u32 s18, 48
	s_cbranch_scc1 .Lsf8_done
	s_add_i32 s18, s18, s33
	s_and_b32 s27, s18, 1
	s_lshr_b32 s19, s18, 1
	s_add_i32 s19, s19, 0x7000
	s_cmp_lt_u32 s19, 0x7000
	s_cbranch_scc0 .Lsf8_down
	s_add_i32 s20, s19, 0xffffc800
	s_lshr_b32 s21, s20, 8
	s_mul_i32 s21, s21, 37
	s_lshr_b32 s21, s21, 8
	s_mul_i32 s28, s21, 0x700
	s_sub_i32 s20, s20, s28
	s_mul_i32 s28, s21, 0x3800000
	s_add_u32 s14, s10, s28
	s_addc_u32 s15, s11, 0
	s_mul_i32 s28, s21, 0x1c00000
	s_add_u32 s28, s28, 0x7800000
	s_add_u32 s16, s86, s28
	s_addc_u32 s17, s87, 0
	s_movk_i32 s24, 0x7000
	s_movk_i32 s25, 0x800
	s_mov_b32 s26, 0x43800000
	s_lshr_b32 s22, s20, 4
	s_mul_i32 s22, s22, 0x2493
	s_lshr_b32 s22, s22, 16
	s_mul_i32 s28, s22, 0x70
	s_sub_i32 s23, s20, s28
	s_mov_b32 s29, 1
	s_branch .Lsf8_dec

; __device__ __forceinline__ void moe_convert(Frame& F, int lo, int hi, int rank, int nrank) {
;     ...
;     for (int it = lo + rank; it < hi; it += nrank) {
;         int r = it; const float* W; unsigned char* WT; int N, ldt, kind, off; float f8s;
;         if (r < 14336) { const int e = r / 1792; r -= e * 1792; W = F.in[IN_WMG] + (size_t)e * 2048 * DFFE; N = DFFE; WT = F.ws + WS_WGU1 + (size_t)e * 14336 * 2048; ldt = 2048; kind = 1; off = 0; f8s = 32.f; }
;         else if ((r -= 14336) < 14336) { const int e = r / 1792; r -= e * 1792; W = F.in[IN_WMU] + (size_t)e * 2048 * DFFE; N = DFFE; WT = F.ws + WS_WGU1 + (size_t)e * 14336 * 2048; ldt = 2048; kind = 1; off = 128; f8s = 256.f; }
;         else { r -= 14336; const int e = r / 1792; r -= e * 1792; W = F.in[IN_WMD] + (size_t)e * DFFE * 2048; N = 2048; WT = F.ws + WS_WDN1 + (size_t)e * 2048 * DFFE; ldt = DFFE; kind = 0; off = 0; f8s = 64.f; }
;         transpose_item_f8(W, N, WT, ldt, kind, off, r, F.lane, f8s);
.Lsf9_loop:
	ds_read_b32 v9, v8
	s_waitcnt lgkmcnt(0)
	v_readfirstlane_b32 s5, v9
	s_cmp_eq_u32 s5, 10
	s_cbranch_scc1 .Lsf9_done
	ds_add_rtn_u32 v9, v8, v18 offset:4
	s_waitcnt lgkmcnt(0)
	v_readfirstlane_b32 s18, v9
	s_cmp_ge_u32 s18, 48
	s_cbranch_scc1 .Lsf9_done
	s_add_i32 s18, s18, s33
	s_and_b32 s27, s18, 1
	s_lshr_b32 s19, s18, 1
	s_add_i32 s19, s19, 0x7000
	s_cmp_lt_u32 s19, 0x7000
	s_cbranch_scc0 .Lsf9_down
	s_add_i32 s20, s19, 0xffffc800
	s_lshr_b32 s21, s20, 8
	s_mul_i32 s21, s21, 37
	s_lshr_b32 s21, s21, 8
	s_mul_i32 s28, s21, 0x700
	s_sub_i32 s20, s20, s28
	s_mul_i32 s28, s21, 0x3800000
	s_add_u32 s14, s10, s28
	s_addc_u32 s15, s11, 0
	s_mul_i32 s28, s21, 0x1c00000
	s_add_u32 s28, s28, 0x7800000
	s_add_u32 s16, s86, s28
	s_addc_u32 s17, s87, 0
	s_movk_i32 s24, 0x7000
	s_movk_i32 s25, 0x800
	s_mov_b32 s26, 0x43800000
	s_lshr_b32 s22, s20, 4
	s_mul_i32 s22, s22, 0x2493
	s_lshr_b32 s22, s22, 16
	s_mul_i32 s28, s22, 0x70
	s_sub_i32 s23, s20, s28
	s_mov_b32 s29, 1
	s_branch .Lsf9_dec

; __device__ __forceinline__ void moe_convert(Frame& F, int lo, int hi, int rank, int nrank) {
;     ...
;     for (int it = lo + rank; it < hi; it += nrank) {
;         int r = it; const float* W; unsigned char* WT; int N, ldt, kind, off; float f8s;
;         if (r < 14336) { const int e = r / 1792; r -= e * 1792; W = F.in[IN_WMG] + (size_t)e * 2048 * DFFE; N = DFFE; WT = F.ws + WS_WGU1 + (size_t)e * 14336 * 2048; ldt = 2048; kind = 1; off = 0; f8s = 32.f; }
;         else if ((r -= 14336) < 14336) { const int e = r / 1792; r -= e * 1792; W = F.in[IN_WMU] + (size_t)e * 2048 * DFFE; N = DFFE; WT = F.ws + WS_WGU1 + (size_t)e * 14336 * 2048; ldt = 2048; kind = 1; off = 128; f8s = 256.f; }
;         else { r -= 14336; const int e = r / 1792; r -= e * 1792; W = F.in[IN_WMD] + (size_t)e * DFFE * 2048; N = 2048; WT = F.ws + WS_WDN1 + (size_t)e * 2048 * DFFE; ldt = DFFE; kind = 0; off = 0; f8s = 64.f; }
;         transpose_item_f8(W, N, WT, ldt, kind, off, r, F.lane, f8s);
.Lsf10_loop:
	ds_read_b32 v9, v8
	s_waitcnt lgkmcnt(0)
	v_readfirstlane_b32 s5, v9
	s_cmp_eq_u32 s5, 11
	s_cbranch_scc1 .Lsf10_done
	ds_add_rtn_u32 v9, v8, v18 offset:4
	s_waitcnt lgkmcnt(0)
	v_readfirstlane_b32 s18, v9
	s_cmp_ge_u32 s18, 48
	s_cbranch_scc1 .Lsf10_done
	s_add_i32 s18, s18, s33
	s_and_b32 s27, s18, 1
	s_lshr_b32 s19, s18, 1
	s_add_i32 s19, s19, 0x7000
	s_cmp_lt_u32 s19, 0x7000
	s_cbranch_scc0 .Lsf10_down
	s_add_i32 s20, s19, 0xffffc800
	s_lshr_b32 s21, s20, 8
	s_mul_i32 s21, s21, 37
	s_lshr_b32 s21, s21, 8
	s_mul_i32 s28, s21, 0x700
	s_sub_i32 s20, s20, s28
	s_mul_i32 s28, s21, 0x3800000
	s_add_u32 s14, s10, s28
	s_addc_u32 s15, s11, 0
	s_mul_i32 s28, s21, 0x1c00000
	s_add_u32 s28, s28, 0x7800000
	s_add_u32 s16, s86, s28
	s_addc_u32 s17, s87, 0
	s_movk_i32 s24, 0x7000
	s_movk_i32 s25, 0x800
	s_mov_b32 s26, 0x43800000
	s_lshr_b32 s22, s20, 4
	s_mul_i32 s22, s22, 0x2493
	s_lshr_b32 s22, s22, 16
	s_mul_i32 s28, s22, 0x70
	s_sub_i32 s23, s20, s28
	s_mov_b32 s29, 1
	s_branch .Lsf10_dec

; __device__ __forceinline__ void moe_convert(Frame& F, int lo, int hi, int rank, int nrank) {
;     ...
;     for (int it = lo + rank; it < hi; it += nrank) {
;         int r = it; const float* W; unsigned char* WT; int N, ldt, kind, off; float f8s;
;         if (r < 14336) { const int e = r / 1792; r -= e * 1792; W = F.in[IN_WMG] + (size_t)e * 2048 * DFFE; N = DFFE; WT = F.ws + WS_WGU1 + (size_t)e * 14336 * 2048; ldt = 2048; kind = 1; off = 0; f8s = 32.f; }
;         else if ((r -= 14336) < 14336) { const int e = r / 1792; r -= e * 1792; W = F.in[IN_WMU] + (size_t)e * 2048 * DFFE; N = DFFE; WT = F.ws + WS_WGU1 + (size_t)e * 14336 * 2048; ldt = 2048; kind = 1; off = 128; f8s = 256.f; }
;         else { r -= 14336; const int e = r / 1792; r -= e * 1792; W = F.in[IN_WMD] + (size_t)e * DFFE * 2048; N = 2048; WT = F.ws + WS_WDN1 + (size_t)e * 2048 * DFFE; ldt = DFFE; kind = 0; off = 0; f8s = 64.f; }
;         transpose_item_f8(W, N, WT, ldt, kind, off, r, F.lane, f8s);
.Lsf11_loop:
	ds_read_b32 v9, v8
	s_waitcnt lgkmcnt(0)
	v_readfirstlane_b32 s5, v9
	s_cmp_eq_u32 s5, 12
	s_cbranch_scc1 .Lsf11_done
	ds_add_rtn_u32 v9, v8, v18 offset:4
	s_waitcnt lgkmcnt(0)
	v_readfirstlane_b32 s18, v9
	s_cmp_ge_u32 s18, 48
	s_cbranch_scc1 .Lsf11_done
	s_add_i32 s18, s18, s33
	s_and_b32 s27, s18, 1
	s_lshr_b32 s19, s18, 1
	s_add_i32 s19, s19, 0x7000
	s_cmp_lt_u32 s19, 0x7000
	s_cbranch_scc0 .Lsf11_down
	s_add_i32 s20, s19, 0xffffc800
	s_lshr_b32 s21, s20, 8
	s_mul_i32 s21, s21, 37
	s_lshr_b32 s21, s21, 8
	s_mul_i32 s28, s21, 0x700
	s_sub_i32 s20, s20, s28
	s_mul_i32 s28, s21, 0x3800000
	s_add_u32 s14, s10, s28
	s_addc_u32 s15, s11, 0
	s_mul_i32 s28, s21, 0x1c00000
	s_add_u32 s28, s28, 0x7800000
	s_add_u32 s16, s86, s28
	s_addc_u32 s17, s87, 0
	s_movk_i32 s24, 0x7000
	s_movk_i32 s25, 0x800
	s_mov_b32 s26, 0x43800000
	s_lshr_b32 s22, s20, 4
	s_mul_i32 s22, s22, 0x2493
	s_lshr_b32 s22, s22, 16
	s_mul_i32 s28, s22, 0x70
	s_sub_i32 s23, s20, s28
	s_mov_b32 s29, 1
	s_branch .Lsf11_dec

; __device__ __forceinline__ void moe_convert(Frame& F, int lo, int hi, int rank, int nrank) {
;     ...
;     for (int it = lo + rank; it < hi; it += nrank) {
;         int r = it; const float* W; unsigned char* WT; int N, ldt, kind, off; float f8s;
;         if (r < 14336) { const int e = r / 1792; r -= e * 1792; W = F.in[IN_WMG] + (size_t)e * 2048 * DFFE; N = DFFE; WT = F.ws + WS_WGU1 + (size_t)e * 14336 * 2048; ldt = 2048; kind = 1; off = 0; f8s = 32.f; }
;         else if ((r -= 14336) < 14336) { const int e = r / 1792; r -= e * 1792; W = F.in[IN_WMU] + (size_t)e * 2048 * DFFE; N = DFFE; WT = F.ws + WS_WGU1 + (size_t)e * 14336 * 2048; ldt = 2048; kind = 1; off = 128; f8s = 256.f; }
;         else { r -= 14336; const int e = r / 1792; r -= e * 1792; W = F.in[IN_WMD] + (size_t)e * DFFE * 2048; N = 2048; WT = F.ws + WS_WDN1 + (size_t)e * 2048 * DFFE; ldt = DFFE; kind = 0; off = 0; f8s = 64.f; }
;         transpose_item_f8(W, N, WT, ldt, kind, off, r, F.lane, f8s);
.Lsf12_loop:
	ds_read_b32 v9, v8
	s_waitcnt lgkmcnt(0)
	v_readfirstlane_b32 s5, v9
	s_cmp_eq_u32 s5, 13
	s_cbranch_scc1 .Lsf12_done
	ds_add_rtn_u32 v9, v8, v18 offset:4
	s_waitcnt lgkmcnt(0)
	v_readfirstlane_b32 s18, v9
	s_cmp_ge_u32 s18, 48
	s_cbranch_scc1 .Lsf12_done
	s_add_i32 s18, s18, s33
	s_and_b32 s27, s18, 1
	s_lshr_b32 s19, s18, 1
	s_add_i32 s19, s19, 0x7000
	s_cmp_lt_u32 s19, 0x7000
	s_cbranch_scc0 .Lsf12_down
	s_add_i32 s20, s19, 0xffffc800
	s_lshr_b32 s21, s20, 8
	s_mul_i32 s21, s21, 37
	s_lshr_b32 s21, s21, 8
	s_mul_i32 s28, s21, 0x700
	s_sub_i32 s20, s20, s28
	s_mul_i32 s28, s21, 0x3800000
	s_add_u32 s14, s10, s28
	s_addc_u32 s15, s11, 0
	s_mul_i32 s28, s21, 0x1c00000
	s_add_u32 s28, s28, 0x7800000
	s_add_u32 s16, s86, s28
	s_addc_u32 s17, s87, 0
	s_movk_i32 s24, 0x7000
	s_movk_i32 s25, 0x800
	s_mov_b32 s26, 0x43800000
	s_lshr_b32 s22, s20, 4
	s_mul_i32 s22, s22, 0x2493
	s_lshr_b32 s22, s22, 16
	s_mul_i32 s28, s22, 0x70
	s_sub_i32 s23, s20, s28
	s_mov_b32 s29, 1
	s_branch .Lsf12_dec

; __device__ __forceinline__ void moe_convert(Frame& F, int lo, int hi, int rank, int nrank) {
;     ...
;     for (int it = lo + rank; it < hi; it += nrank) {
;         int r = it; const float* W; unsigned char* WT; int N, ldt, kind, off; float f8s;
;         if (r < 14336) { const int e = r / 1792; r -= e * 1792; W = F.in[IN_WMG] + (size_t)e * 2048 * DFFE; N = DFFE; WT = F.ws + WS_WGU1 + (size_t)e * 14336 * 2048; ldt = 2048; kind = 1; off = 0; f8s = 32.f; }
;         else if ((r -= 14336) < 14336) { const int e = r / 1792; r -= e * 1792; W = F.in[IN_WMU] + (size_t)e * 2048 * DFFE; N = DFFE; WT = F.ws + WS_WGU1 + (size_t)e * 14336 * 2048; ldt = 2048; kind = 1; off = 128; f8s = 256.f; }
;         else { r -= 14336; const int e = r / 1792; r -= e * 1792; W = F.in[IN_WMD] + (size_t)e * DFFE * 2048; N = 2048; WT = F.ws + WS_WDN1 + (size_t)e * 2048 * DFFE; ldt = DFFE; kind = 0; off = 0; f8s = 64.f; }
;         transpose_item_f8(W, N, WT, ldt, kind, off, r, F.lane, f8s);
.Lsf13_loop:
	ds_read_b32 v9, v8
	s_waitcnt lgkmcnt(0)
	v_readfirstlane_b32 s5, v9
	s_cmp_eq_u32 s5, 14
	s_cbranch_scc1 .Lsf13_done
	ds_add_rtn_u32 v9, v8, v18 offset:4
	s_waitcnt lgkmcnt(0)
	v_readfirstlane_b32 s18, v9
	s_cmp_ge_u32 s18, 48
	s_cbranch_scc1 .Lsf13_done
	s_add_i32 s18, s18, s33
	s_and_b32 s27, s18, 1
	s_lshr_b32 s19, s18, 1
	s_add_i32 s19, s19, 0x7000
	s_cmp_lt_u32 s19, 0x7000
	s_cbranch_scc0 .Lsf13_down
	s_add_i32 s20, s19, 0xffffc800
	s_lshr_b32 s21, s20, 8
	s_mul_i32 s21, s21, 37
	s_lshr_b32 s21, s21, 8
	s_mul_i32 s28, s21, 0x700
	s_sub_i32 s20, s20, s28
	s_mul_i32 s28, s21, 0x3800000
	s_add_u32 s14, s10, s28
	s_addc_u32 s15, s11, 0
	s_mul_i32 s28, s21, 0x1c00000
	s_add_u32 s28, s28, 0x7800000
	s_add_u32 s16, s86, s28
	s_addc_u32 s17, s87, 0
	s_movk_i32 s24, 0x7000
	s_movk_i32 s25, 0x800
	s_mov_b32 s26, 0x43800000
	s_lshr_b32 s22, s20, 4
	s_mul_i32 s22, s22, 0x2493
	s_lshr_b32 s22, s22, 16
	s_mul_i32 s28, s22, 0x70
	s_sub_i32 s23, s20, s28
	s_mov_b32 s29, 1
	s_branch .Lsf13_dec

; __device__ __forceinline__ void moe_convert(Frame& F, int lo, int hi, int rank, int nrank) {
;     ...
;     for (int it = lo + rank; it < hi; it += nrank) {
;         int r = it; const float* W; unsigned char* WT; int N, ldt, kind, off; float f8s;
;         if (r < 14336) { const int e = r / 1792; r -= e * 1792; W = F.in[IN_WMG] + (size_t)e * 2048 * DFFE; N = DFFE; WT = F.ws + WS_WGU1 + (size_t)e * 14336 * 2048; ldt = 2048; kind = 1; off = 0; f8s = 32.f; }
;         else if ((r -= 14336) < 14336) { const int e = r / 1792; r -= e * 1792; W = F.in[IN_WMU] + (size_t)e * 2048 * DFFE; N = DFFE; WT = F.ws + WS_WGU1 + (size_t)e * 14336 * 2048; ldt = 2048; kind = 1; off = 128; f8s = 256.f; }
;         else { r -= 14336; const int e = r / 1792; r -= e * 1792; W = F.in[IN_WMD] + (size_t)e * DFFE * 2048; N = 2048; WT = F.ws + WS_WDN1 + (size_t)e * 2048 * DFFE; ldt = DFFE; kind = 0; off = 0; f8s = 64.f; }
;         transpose_item_f8(W, N, WT, ldt, kind, off, r, F.lane, f8s);
.Lsf14_loop:
	ds_read_b32 v9, v8
	s_waitcnt lgkmcnt(0)
	v_readfirstlane_b32 s5, v9
	s_cmp_eq_u32 s5, 15
	s_cbranch_scc1 .Lsf14_done
	ds_add_rtn_u32 v9, v8, v18 offset:4
	s_waitcnt lgkmcnt(0)
	v_readfirstlane_b32 s18, v9
	s_cmp_ge_u32 s18, 48
	s_cbranch_scc1 .Lsf14_done
	s_add_i32 s18, s18, s33
	s_and_b32 s27, s18, 1
	s_lshr_b32 s19, s18, 1
	s_add_i32 s19, s19, 0x7000
	s_cmp_lt_u32 s19, 0x7000
	s_cbranch_scc0 .Lsf14_down
	s_add_i32 s20, s19, 0xffffc800
	s_lshr_b32 s21, s20, 8
	s_mul_i32 s21, s21, 37
	s_lshr_b32 s21, s21, 8
	s_mul_i32 s28, s21, 0x700
	s_sub_i32 s20, s20, s28
	s_mul_i32 s28, s21, 0x3800000
	s_add_u32 s14, s10, s28
	s_addc_u32 s15, s11, 0
	s_mul_i32 s28, s21, 0x1c00000
	s_add_u32 s28, s28, 0x7800000
	s_add_u32 s16, s86, s28
	s_addc_u32 s17, s87, 0
	s_movk_i32 s24, 0x7000
	s_movk_i32 s25, 0x800
	s_mov_b32 s26, 0x43800000
	s_lshr_b32 s22, s20, 4
	s_mul_i32 s22, s22, 0x2493
	s_lshr_b32 s22, s22, 16
	s_mul_i32 s28, s22, 0x70
	s_sub_i32 s23, s20, s28
	s_mov_b32 s29, 1
	s_branch .Lsf14_dec

; __device__ __forceinline__ void moe_convert(Frame& F, int lo, int hi, int rank, int nrank) {
;     if (MOE_DMA) { moe_convert_dma(F, lo, hi, rank, nrank); return; }
;     for (int it = lo + rank; it < hi; it += nrank) {
;         int r = it; const float* W; unsigned char* WT; int N, ldt, kind, off; float f8s;
;         if (r < 14336) { const int e = r / 1792; r -= e * 1792; W = F.in[IN_WMG] + (size_t)e * 2048 * DFFE; N = DFFE; WT = F.ws + WS_WGU1 + (size_t)e * 14336 * 2048; ldt = 2048; kind = 1; off = 0; f8s = 32.f; }
;         else if ((r -= 14336) < 14336) { const int e = r / 1792; r -= e * 1792; W = F.in[IN_WMU] + (size_t)e * 2048 * DFFE; N = DFFE; WT = F.ws + WS_WGU1 + (size_t)e * 14336 * 2048; ldt = 2048; kind = 1; off = 128; f8s = 256.f; }
;         else { r -= 14336; const int e = r / 1792; r -= e * 1792; W = F.in[IN_WMD] + (size_t)e * DFFE * 2048; N = 2048; WT = F.ws + WS_WDN1 + (size_t)e * 2048 * DFFE; ldt = DFFE; kind = 0; off = 0; f8s = 64.f; }
;         transpose_item_f8(W, N, WT, ldt, kind, off, r, F.lane, f8s);
.Lsf15_notw0:
	s_cmp_gt_u32 s4, 3
	s_cbranch_scc1 .Lsf15_skip
	v_mov_b32_e32 v8, 0x20020
	ds_read_b32 v9, v8 offset:4
	v_mbcnt_lo_u32_b32 v2, -1, 0
	v_mbcnt_hi_u32_b32 v2, -1, v2
	s_waitcnt lgkmcnt(0)
	v_readfirstlane_b32 s5, v9
	s_cmp_ge_u32 s5, 48
	s_cbranch_scc1 .Lsf15_skip
	s_add_i32 s5, s4, -1
	s_lshl_b32 s5, s5, 14
	v_lshl_add_u32 v7, v2, 4, s5
	ds_write_b128 v7, v[160:163] offset:0
	ds_write_b128 v7, v[164:167] offset:1024
	ds_write_b128 v7, v[168:171] offset:2048
	ds_write_b128 v7, v[172:175] offset:3072
	ds_write_b128 v7, v[176:179] offset:4096
	ds_write_b128 v7, v[180:183] offset:5120
	ds_write_b128 v7, v[184:187] offset:6144
	ds_write_b128 v7, v[188:191] offset:7168
	ds_write_b128 v7, v[192:195] offset:8192
	ds_write_b128 v7, v[196:199] offset:9216
	ds_write_b128 v7, v[200:203] offset:10240
	ds_write_b128 v7, v[204:207] offset:11264
	ds_write_b128 v7, v[208:211] offset:12288
	ds_write_b128 v7, v[212:215] offset:13312
	ds_write_b128 v7, v[216:219] offset:14336
	ds_write_b128 v7, v[220:223] offset:15360
	v_readlane_b32 s6, v247, 0
	v_readlane_b32 s7, v247, 1
	s_load_dwordx2 s[10:11], s[6:7], 0xc0
	s_load_dwordx2 s[12:13], s[6:7], 0xc8
	v_readlane_b32 s33, v247, 6
	v_mov_b32_e32 v3, 0x43e00000
	v_cmp_eq_u32_e32 vcc, 0, v2
	s_mul_i32 s33, s33, 48
	s_nop 1
	v_cndmask_b32_e64 v18, 0, 1, vcc
	s_waitcnt lgkmcnt(0)
.Lsf15_loop:
	ds_add_rtn_u32 v9, v8, v18 offset:4
	s_waitcnt lgkmcnt(0)
	v_readfirstlane_b32 s18, v9
	s_cmp_ge_u32 s18, 48
	s_cbranch_scc1 .Lsf15_done
	s_add_i32 s18, s18, s33
	s_and_b32 s27, s18, 1
	s_lshr_b32 s19, s18, 1
	s_add_i32 s19, s19, 0x7000
	s_cmp_lt_u32 s19, 0x7000
	s_cbranch_scc0 .Lsf15_down
	s_add_i32 s20, s19, 0xffffc800
	s_lshr_b32 s21, s20, 8
	s_mul_i32 s21, s21, 37
	s_lshr_b32 s21, s21, 8
	s_mul_i32 s28, s21, 0x700
	s_sub_i32 s20, s20, s28
	s_mul_i32 s28, s21, 0x3800000
	s_add_u32 s14, s10, s28
	s_addc_u32 s15, s11, 0
	s_mul_i32 s28, s21, 0x1c00000
	s_add_u32 s28, s28, 0x7800000
	s_add_u32 s16, s86, s28
	s_addc_u32 s17, s87, 0
	s_movk_i32 s24, 0x7000
	s_movk_i32 s25, 0x800
	s_mov_b32 s26, 0x43800000
	s_lshr_b32 s22, s20, 4
	s_mul_i32 s22, s22, 0x2493
	s_lshr_b32 s22, s22, 16
	s_mul_i32 s28, s22, 0x70
	s_sub_i32 s23, s20, s28
	s_mov_b32 s29, 1
	s_branch .Lsf15_dec
